# baseline (speedup 1.0000x reference)
_Z8k_layer1PKiS0_PKfPK6__halfS2_S2_P7__half2:
	s_load_dwordx4 s[4:7], s[0:1], 0x0
	s_load_dwordx2 s[8:9], s[0:1], 0x18
	s_load_dwordx2 s[26:27], s[0:1], 0x28
	s_load_dwordx2 s[28:29], s[0:1], 0x20
	s_lshl_b32 s12, s2, 5
	s_ashr_i32 s13, s12, 31
	s_min_i32 s14, s12, 0x18680
	s_lshl_b64 s[2:3], s[12:13], 2
	s_waitcnt lgkmcnt(0)
	s_add_u32 s2, s6, s2
	s_addc_u32 s3, s7, s3
	s_ashr_i32 s15, s14, 31
	s_lshl_b64 s[14:15], s[14:15], 2
	s_add_u32 s6, s6, s14
	s_addc_u32 s7, s7, s15
	s_load_dword s10, s[2:3], 0x0
	s_load_dword s11, s[6:7], 0x80
	v_lshlrev_b32_e32 v91, 2, v0
	global_load_dword v90, v91, s[26:27]
	v_lshrrev_b32_e32 v1, 1, v0
	v_or_b32_e32 v20, s12, v1
	s_mov_b32 s6, 0x186a0
	v_and_b32_e32 v23, 1, v0
	v_cmp_gt_i32_e32 vcc, s6, v20
	v_mov_b32_e32 v2, 0
	v_mov_b32_e32 v22, 0
	v_mov_b32_e32 v3, 0
	v_mov_b32_e32 v4, 0
	v_mov_b32_e32 v5, 0
	v_mov_b32_e32 v16, 0
	v_mov_b32_e32 v17, 0
	s_and_saveexec_b64 s[6:7], vcc
	s_cbranch_execz .LBB2_2
	s_load_dwordx2 s[12:13], s[0:1], 0x10
	v_ashrrev_i32_e32 v21, 31, v20
	v_lshlrev_b32_e32 v1, 2, v1
	v_lshlrev_b32_e32 v4, 4, v23
	global_load_dwordx2 v[16:17], v1, s[2:3]
	s_waitcnt lgkmcnt(0)
	v_lshl_add_u64 v[2:3], v[20:21], 2, s[12:13]
	v_lshl_or_b32 v1, v20, 5, v4
	global_load_dword v22, v[2:3], off
	s_nop 0
	global_load_dwordx4 v[2:5], v1, s[8:9]

.LBB2_29:
	v_cmp_gt_u32_e64 s[2:3], 32, v0
	s_and_saveexec_b64 s[6:7], s[2:3]
	s_cbranch_execz .LBB2_31
	v_lshlrev_b32_e32 v1, 2, v0
	v_and_b32_e32 v0, 15, v0
	v_lshlrev_b32_e32 v0, 2, v0
	s_movk_i32 s2, 0xc0
	v_and_or_b32 v0, v1, s2, v0
	s_waitcnt vmcnt(0)
	ds_write_b32 v0, v90 offset:6144

.LBB2_62:
	v_lshlrev_b32_e32 v21, 5, v23
	global_load_dwordx4 v[24:27], v21, s[28:29]
	global_load_dwordx4 v[28:31], v21, s[28:29] offset:16
	v_subrev_u32_e32 v10, s10, v16
	v_sub_u32_e32 v11, v17, v16
	v_lshlrev_b32_e32 v10, 2, v10
	v_lshlrev_b32_e32 v9, 4, v23
	s_mov_b64 s[16:17], exec
	v_cmp_le_u32_e32 vcc, 8, v11
	s_mov_b64 s[12:13], vcc
	s_mov_b64 exec, vcc
	s_cbranch_execz .Lk3_drainA
	ds_read2_b32 v[12:13], v10 offset1:1
	ds_read2_b32 v[14:15], v10 offset0:2 offset1:3
	ds_read2_b32 v[16:17], v10 offset0:4 offset1:5
	ds_read2_b32 v[18:19], v10 offset0:6 offset1:7
	v_add_u32_e32 v10, 32, v10
	v_subrev_u32_e32 v11, 8, v11
	s_waitcnt lgkmcnt(0)
	v_lshl_or_b32 v12, v12, 5, v9
	v_lshl_or_b32 v13, v13, 5, v9
	v_lshl_or_b32 v14, v14, 5, v9
	v_lshl_or_b32 v15, v15, 5, v9
	v_lshl_or_b32 v16, v16, 5, v9
	v_lshl_or_b32 v17, v17, 5, v9
	v_lshl_or_b32 v18, v18, 5, v9
	v_lshl_or_b32 v19, v19, 5, v9
	global_load_dwordx4 v[32:35], v12, s[8:9]
	global_load_dwordx4 v[36:39], v13, s[8:9]
	global_load_dwordx4 v[40:43], v14, s[8:9]
	global_load_dwordx4 v[44:47], v15, s[8:9]
	global_load_dwordx4 v[48:51], v16, s[8:9]
	global_load_dwordx4 v[52:55], v17, s[8:9]
	global_load_dwordx4 v[56:59], v18, s[8:9]
	global_load_dwordx4 v[60:63], v19, s[8:9]

.Lk3_fin:
	s_waitcnt vmcnt(0)
	v_mov_b64_e32 v[8:9], v[0:1]
	v_mov_b64_e32 v[10:11], v[2:3]
	v_mov_b64_e32 v[12:13], v[4:5]
	v_mov_b64_e32 v[14:15], v[6:7]
	v_mov_b64_e32 v[0:1], v[24:25]
	v_mov_b64_e32 v[2:3], v[26:27]
	v_mov_b64_e32 v[4:5], v[28:29]
	v_mov_b64_e32 v[6:7], v[30:31]
	v_lshlrev_b32_e32 v21, 5, v23
	s_waitcnt lgkmcnt(0)
	s_branch .Lk3_ep

.Lk3_ep:
	v_mbcnt_lo_u32_b32 v28, -1, 0
	ds_read_b128 v[30:33], v21 offset:6144
	ds_read_b128 v[34:37], v21 offset:6160
	s_waitcnt vmcnt(2)
	ds_read_b128 v[16:19], v21 offset:6208
	ds_read_b128 v[24:27], v21 offset:6224
	v_mbcnt_hi_u32_b32 v21, -1, v28
	v_and_b32_e32 v29, 64, v21
	v_xor_b32_e32 v28, 1, v21
	v_add_u32_e32 v29, 64, v29
	v_cmp_lt_i32_e32 vcc, v28, v29
	s_waitcnt lgkmcnt(1)
	v_mov_b32_e32 v29, v16
	v_mov_b32_e32 v16, v31
	v_cndmask_b32_e32 v21, v21, v28, vcc
	v_mov_b32_e32 v28, v30
	v_mov_b32_e32 v30, v32
	v_mov_b32_e32 v31, v18
	v_mov_b32_e32 v18, v33
	v_mov_b32_e32 v32, v34
	s_waitcnt lgkmcnt(0)
	v_mov_b32_e32 v33, v24
	v_mov_b32_e32 v24, v35
	v_mov_b32_e32 v34, v36
	v_mov_b32_e32 v35, v26
	v_mov_b32_e32 v26, v37
	v_lshlrev_b32_e32 v21, 2, v21
	v_cmp_eq_u32_e32 vcc, 0, v23
	s_waitcnt vmcnt(1)
	v_fma_f32 v0, v22, v8, v0
	v_fma_f32 v1, v22, v9, v1
	v_max_f32_e32 v0, 0, v0
	v_fma_f32 v8, v22, v10, v2
	v_fmac_f32_e32 v3, v22, v11
	v_max_f32_e32 v2, 0, v1
	v_pk_fma_f32 v[0:1], v[28:29], v[0:1], 0 op_sel_hi:[1,0,0]
	s_waitcnt vmcnt(0)
	v_fma_f32 v9, v22, v12, v4
	v_fma_f32 v5, v22, v13, v5
	v_max_f32_e32 v4, 0, v8
	v_pk_fma_f32 v[0:1], v[16:17], v[2:3], v[0:1] op_sel_hi:[1,0,1]
	v_fma_f32 v11, v22, v14, v6
	v_fmac_f32_e32 v7, v22, v15
	v_max_f32_e32 v6, 0, v3
	v_pk_fma_f32 v[0:1], v[30:31], v[4:5], v[0:1] op_sel_hi:[1,0,1]
	v_max_f32_e32 v8, 0, v9
	v_pk_fma_f32 v[0:1], v[18:19], v[6:7], v[0:1] op_sel_hi:[1,0,1]
	v_max_f32_e32 v10, 0, v5
	v_pk_fma_f32 v[0:1], v[32:33], v[8:9], v[0:1] op_sel_hi:[1,0,1]
	v_max_f32_e32 v12, 0, v11
	v_pk_fma_f32 v[0:1], v[24:25], v[10:11], v[0:1] op_sel_hi:[1,0,1]
	v_max_f32_e32 v14, 0, v7
	v_pk_fma_f32 v[0:1], v[34:35], v[12:13], v[0:1] op_sel_hi:[1,0,1]
	s_nop 0
	v_pk_fma_f32 v[0:1], v[26:27], v[14:15], v[0:1] op_sel_hi:[1,0,1]
	ds_bpermute_b32 v2, v21, v0
	ds_bpermute_b32 v3, v21, v1
	s_and_b64 exec, exec, vcc
	s_cbranch_execz .LBB2_82
	s_waitcnt lgkmcnt(0)
	v_pk_add_f32 v[0:1], v[0:1], v[2:3]
	v_ashrrev_i32_e32 v21, 31, v20
	v_pk_mul_f32 v[0:1], v[22:23], v[0:1] op_sel_hi:[0,1]
	v_cvt_pk_f16_f32 v2, v0, v1
	v_lshl_add_u64 v[0:1], v[20:21], 2, s[4:5]
	global_store_dword v[0:1], v2, off
